# baseline (speedup 1.0000x reference)
_Z11knrm_kernelPKfS0_PKiS2_S0_Pf:
	v_lshrrev_b32_e32 v1, 6, v0
	s_load_dwordx8 s[4:11], s[0:1], 0x0
	s_load_dwordx4 s[12:15], s[0:1], 0x20
	v_lshlrev_b32_e32 v2, 2, v0
	v_bfe_u32 v3, v0, 2, 2
	v_lshlrev_b32_e32 v124, 5, v1
	v_and_or_b32 v98, v2, 12, v3
	v_lshl_or_b32 v8, s2, 8, v124
	v_or_b32_e32 v2, v8, v98
	v_ashrrev_i32_e32 v3, 31, v2
	s_waitcnt lgkmcnt(0)
	v_lshl_add_u64 v[4:5], v[2:3], 2, s[10:11]
	v_or_b32_e32 v2, 24, v2
	v_and_or_b32 v6, v98, 7, v8
	v_ashrrev_i32_e32 v3, 31, v2
	s_movk_i32 s0, 0x160
	v_ashrrev_i32_e32 v7, 31, v6
	v_lshl_add_u64 v[2:3], v[2:3], 2, s[10:11]
	v_lshrrev_b32_e32 v121, 5, v0
	v_cmp_gt_u32_e64 s[0:1], s0, v0
	v_lshl_add_u64 v[6:7], v[6:7], 2, s[10:11]
	global_load_dword v125, v[4:5], off
	global_load_dword v126, v[6:7], off offset:64
	global_load_dword v127, v[2:3], off
	v_cndmask_b32_e64 v2, 10, v121, s[0:1]
	v_lshlrev_b32_e32 v2, 2, v2
	s_lshl_b32 s3, s2, 5
	v_and_b32_e32 v122, 31, v0
	global_load_dword v118, v2, s[12:13]
	v_or_b32_e32 v2, s3, v122
	v_ashrrev_i32_e32 v3, 31, v2
	v_lshl_add_u64 v[2:3], v[2:3], 2, s[8:9]
	v_lshrrev_b32_e32 v100, 4, v0
	global_load_dword v119, v[2:3], off
	v_or_b32_e32 v2, s3, v100
	s_movk_i32 s3, 0x4b0
	v_and_b32_e32 v123, 15, v0
	s_mov_b32 s19, 0x20000
	v_mul_lo_u32 v2, v2, s3
	v_and_b32_e32 v120, 63, v0
	s_mov_b64 s[16:17], s[6:7]
	s_and_b32 s5, s5, 0xffff
	s_mov_b32 s6, 0x960000
	s_mov_b32 s7, s19
	v_lshl_add_u32 v3, v123, 4, v2
	v_mul_lo_u32 v99, v8, s3
	v_lshlrev_b32_e32 v132, 4, v120
	buffer_load_dwordx4 v[90:93], v3, s[4:7], 0 offen nt
	buffer_load_dwordx4 v[86:89], v3, s[4:7], 0 offen offset:256 nt
	buffer_load_dwordx4 v[82:85], v3, s[4:7], 0 offen offset:512 nt
	buffer_load_dwordx4 v[78:81], v3, s[4:7], 0 offen offset:768 nt
	v_min_u32_e32 v3, 10, v123
	v_add_u32_e32 v38, v99, v132
	s_mov_b32 s18, 0x4b00000
	s_and_b32 s17, s17, 0xffff
	v_lshl_add_u32 v2, v3, 4, v2
	v_add_u32_e32 v6, 0x1000, v38
	v_add_u32_e32 v18, 0x2000, v38
	v_add_u32_e32 v39, 0x3000, v38
	v_add_u32_e32 v50, 0x4000, v38
	buffer_load_dwordx4 v[94:97], v2, s[4:7], 0 offen offset:1024 nt
	s_nop 0
	buffer_load_dwordx4 v[2:5], v38, s[16:19], 0 offen nt
	buffer_load_dwordx4 v[14:17], v38, s[16:19], 0 offen offset:1024 nt
	buffer_load_dwordx4 v[34:37], v38, s[16:19], 0 offen offset:2048 nt
	buffer_load_dwordx4 v[46:49], v38, s[16:19], 0 offen offset:3072 nt
	buffer_load_dwordx4 v[54:57], v6, s[16:19], 0 offen nt
	buffer_load_dwordx4 v[58:61], v6, s[16:19], 0 offen offset:1024 nt
	buffer_load_dwordx4 v[62:65], v6, s[16:19], 0 offen offset:2048 nt
	buffer_load_dwordx4 v[66:69], v6, s[16:19], 0 offen offset:3072 nt
	buffer_load_dwordx4 v[70:73], v18, s[16:19], 0 offen nt
	buffer_load_dwordx4 v[74:77], v18, s[16:19], 0 offen offset:1024 nt
	s_nop 0
	buffer_load_dwordx4 v[6:9], v18, s[16:19], 0 offen offset:2048 nt
	buffer_load_dwordx4 v[10:13], v18, s[16:19], 0 offen offset:3072 nt
	s_nop 0
	buffer_load_dwordx4 v[18:21], v39, s[16:19], 0 offen nt
	buffer_load_dwordx4 v[22:25], v39, s[16:19], 0 offen offset:1024 nt
	buffer_load_dwordx4 v[26:29], v39, s[16:19], 0 offen offset:2048 nt
	buffer_load_dwordx4 v[30:33], v39, s[16:19], 0 offen offset:3072 nt
	s_nop 0
	buffer_load_dwordx4 v[38:41], v50, s[16:19], 0 offen nt
	buffer_load_dwordx4 v[42:45], v50, s[16:19], 0 offen offset:1024 nt
	v_min_u32_e32 v50, 47, v120
	s_movk_i32 s3, 0x4000
	v_lshlrev_b32_e32 v50, 4, v50
	v_add3_u32 v50, v99, v50, s3
	buffer_load_dwordx4 v[50:53], v50, s[16:19], 0 offen offset:2048 nt
	s_movk_i32 s26, 0x4b00
	s_movk_i32 s27, 0x6f00
	v_add3_u32 v226, v99, v132, s26
	v_min_u32_e32 v229, 23, v120
	v_add_u32_e32 v227, 0x1000, v226
	v_lshlrev_b32_e32 v229, 4, v229
	v_add_u32_e32 v228, 0x2000, v226
	v_add3_u32 v229, v99, v229, s27
	buffer_load_dwordx4 v[186:189], v226, s[16:19], 0 offen nt
	buffer_load_dwordx4 v[190:193], v226, s[16:19], 0 offen offset:1024 nt
	buffer_load_dwordx4 v[194:197], v226, s[16:19], 0 offen offset:2048 nt
	buffer_load_dwordx4 v[198:201], v226, s[16:19], 0 offen offset:3072 nt
	buffer_load_dwordx4 v[202:205], v227, s[16:19], 0 offen nt
	buffer_load_dwordx4 v[206:209], v227, s[16:19], 0 offen offset:1024 nt
	buffer_load_dwordx4 v[210:213], v227, s[16:19], 0 offen offset:2048 nt
	buffer_load_dwordx4 v[214:217], v227, s[16:19], 0 offen offset:3072 nt
	buffer_load_dwordx4 v[218:221], v228, s[16:19], 0 offen nt
	buffer_load_dwordx4 v[222:225], v229, s[16:19], 0 offen nt
	s_mov_b32 s3, 0
	v_mul_u32_u24_e32 v131, 0x2600, v1
	v_cmp_gt_u32_e64 s[4:5], 16, v120
	s_and_saveexec_b64 s[6:7], s[4:5]
	s_movk_i32 s8, 0x260
	v_mov_b32_e32 v102, 0
	v_mad_u32_u24 v101, v120, s8, v131
	v_mov_b32_e32 v103, v102
	ds_write_b64 v101, v[102:103] offset:20056
	s_or_b64 exec, exec, s[6:7]
	v_cmp_lt_u32_e32 vcc, 10, v123
	s_waitcnt vmcnt(32)
	v_mul_f32_e32 v101, v87, v87
	v_mov_b32_e32 v106, v92
	s_waitcnt vmcnt(29)
	v_cndmask_b32_e64 v103, v97, 0, vcc
	v_cndmask_b32_e64 v102, v96, 0, vcc
	v_mov_b32_e32 v96, v91
	v_mov_b32_e32 v97, v83
	v_cndmask_b32_e64 v105, v95, 0, vcc
	v_cndmask_b32_e64 v104, v94, 0, vcc
	v_mov_b32_e32 v94, v90
	v_mov_b32_e32 v95, v82
	v_pk_mul_f32 v[96:97], v[96:97], v[96:97]
	v_mov_b32_e32 v107, v84
	v_fmac_f32_e32 v101, v86, v86
	v_pk_fma_f32 v[94:95], v[94:95], v[94:95], v[96:97]
	v_mov_b32_e32 v108, v93
	v_mov_b32_e32 v109, v85
	v_fmac_f32_e32 v101, v88, v88
	v_pk_fma_f32 v[94:95], v[106:107], v[106:107], v[94:95]
	v_fmac_f32_e32 v101, v89, v89
	v_pk_fma_f32 v[94:95], v[108:109], v[108:109], v[94:95]
	v_mov_b32_e32 v96, v79
	v_add_f32_e32 v94, v94, v101
	v_mov_b32_e32 v97, v105
	v_add_f32_e32 v101, v94, v95
	v_mov_b32_e32 v94, v78
	v_mov_b32_e32 v95, v104
	v_pk_mul_f32 v[96:97], v[96:97], v[96:97]
	s_mov_b32 s21, 0xf800000
	v_pk_fma_f32 v[94:95], v[94:95], v[94:95], v[96:97]
	v_mov_b32_e32 v96, v80
	v_mov_b32_e32 v97, v102
	v_pk_fma_f32 v[94:95], v[96:97], v[96:97], v[94:95]
	v_mov_b32_e32 v96, v81
	v_mov_b32_e32 v97, v103
	v_pk_fma_f32 v[94:95], v[96:97], v[96:97], v[94:95]
	v_mov_b32_e32 v135, 0x260
	v_add_f32_e32 v94, v101, v94
	v_add_f32_e32 v94, v94, v95
	v_mbcnt_lo_u32_b32 v95, -1, 0
	v_mbcnt_hi_u32_b32 v95, -1, v95
	v_and_b32_e32 v97, 64, v95
	v_xor_b32_e32 v96, 1, v95
	v_add_u32_e32 v101, 64, v97
	v_cmp_lt_i32_e32 vcc, v96, v101
	s_movk_i32 s8, 0x260
	v_add_u32_e32 v137, 0x4b00, v99
	v_cndmask_b32_e32 v96, v95, v96, vcc
	v_lshlrev_b32_e32 v97, 2, v96
	ds_bpermute_b32 v96, v97, v94
	s_movk_i32 s10, 0x1b5
	v_mov_b32_e32 v99, 0x36a00
	v_mov_b32_e32 v111, 0x666c0
	v_mov_b32_e32 v113, 0x6d400
	s_waitcnt lgkmcnt(0)
	v_add_f32_e32 v94, v94, v96
	v_xor_b32_e32 v96, 2, v95
	v_cmp_lt_i32_e32 vcc, v96, v101
	v_mov_b32_e32 v115, 0x74140
	s_mov_b32 s20, 0xbeb17218
	v_cndmask_b32_e32 v96, v95, v96, vcc
	v_lshlrev_b32_e32 v128, 2, v96
	ds_bpermute_b32 v96, v128, v94
	s_mov_b32 s22, 0x44132d1f
	v_mov_b32_e32 v161, 0xc47a0000
	s_waitcnt lgkmcnt(0)
	v_add_f32_e32 v94, v94, v96
	v_xor_b32_e32 v96, 4, v95
	v_cmp_lt_i32_e32 vcc, v96, v101
	s_nop 1
	v_cndmask_b32_e32 v96, v95, v96, vcc
	v_lshlrev_b32_e32 v129, 2, v96
	ds_bpermute_b32 v96, v129, v94
	s_waitcnt lgkmcnt(0)
	v_add_f32_e32 v94, v94, v96
	v_xor_b32_e32 v96, 8, v95
	v_cmp_lt_i32_e32 vcc, v96, v101
	s_nop 1
	v_cndmask_b32_e32 v96, v95, v96, vcc
	v_lshlrev_b32_e32 v130, 2, v96
	ds_bpermute_b32 v96, v130, v94
	s_waitcnt lgkmcnt(0)
	v_add_f32_e32 v94, v94, v96
	v_mul_f32_e32 v96, 0x4f800000, v94
	v_cmp_gt_f32_e32 vcc, s21, v94
	s_nop 1
	v_cndmask_b32_e32 v94, v94, v96, vcc
	v_sqrt_f32_e32 v96, v94
	s_nop 0
	v_add_u32_e32 v106, -1, v96
	v_fma_f32 v107, -v106, v96, v94
	v_cmp_ge_f32_e64 s[6:7], 0, v107
	v_add_u32_e32 v107, 1, v96
	s_nop 0
	v_cndmask_b32_e64 v106, v96, v106, s[6:7]
	v_fma_f32 v96, -v107, v96, v94
	v_cmp_lt_f32_e64 s[6:7], 0, v96
	s_nop 1
	v_cndmask_b32_e64 v96, v106, v107, s[6:7]
	v_mul_f32_e32 v106, 0x37800000, v96
	v_cndmask_b32_e32 v96, v96, v106, vcc
	v_cmp_class_f32_e32 vcc, v94, v135
	s_nop 1
	v_cndmask_b32_e32 v94, v96, v94, vcc
	v_add_f32_e32 v96, 0x29e12e13, v94
	v_div_scale_f32 v106, s[6:7], v96, v96, 1.0
	v_rcp_f32_e32 v107, v106
	v_mov_b32_e32 v94, 0
	v_cmp_gt_u32_e64 s[6:7], 48, v120
	v_mov_b32_e32 v116, v94
	v_fma_f32 v108, -v106, v107, 1.0
	v_fmac_f32_e32 v107, v108, v107
	v_div_scale_f32 v108, vcc, 1.0, v96, 1.0
	v_mul_f32_e32 v109, v108, v107
	v_fma_f32 v110, -v106, v109, v108
	v_fmac_f32_e32 v109, v110, v107
	v_fma_f32 v106, -v106, v109, v108
	v_div_fmas_f32 v106, v106, v107, v109
	v_div_fixup_f32 v96, v106, v96, 1.0
	v_lshlrev_b32_e32 v106, 3, v123
	v_pk_mul_f32 v[82:83], v[96:97], v[82:83] op_sel_hi:[0,1]
	v_pk_mul_f32 v[84:85], v[96:97], v[84:85] op_sel_hi:[0,1]
	v_pk_mul_f32 v[78:79], v[96:97], v[78:79] op_sel_hi:[0,1]
	v_pk_mul_f32 v[80:81], v[96:97], v[80:81] op_sel_hi:[0,1]
	v_mad_u32_u24 v100, v100, s8, v106
	v_cvt_pk_f16_f32 v82, v82, v83
	v_cvt_pk_f16_f32 v83, v84, v85
	v_cvt_pk_f16_f32 v78, v78, v79
	v_cvt_pk_f16_f32 v79, v80, v81
	ds_write2_b64 v100, v[82:83], v[78:79] offset0:32 offset1:48
	v_min_u32_e32 v82, 23, v120
	v_mov_b32_e32 v83, 0x2400
	v_lshl_or_b32 v138, v82, 4, v83
	v_xor_b32_e32 v83, 16, v95
	v_cmp_lt_i32_e32 vcc, v83, v101
	v_pk_mul_f32 v[90:91], v[96:97], v[90:91] op_sel_hi:[0,1]
	v_pk_mul_f32 v[92:93], v[96:97], v[92:93] op_sel_hi:[0,1]
	v_cndmask_b32_e32 v83, v95, v83, vcc
	v_lshlrev_b32_e32 v133, 2, v83
	v_xor_b32_e32 v83, 32, v95
	v_pk_mul_f32 v[86:87], v[96:97], v[86:87] op_sel_hi:[0,1]
	v_pk_mul_f32 v[88:89], v[96:97], v[88:89] op_sel_hi:[0,1]
	v_pk_mul_f32 v[78:79], v[96:97], v[104:105] op_sel_hi:[0,1]
	v_pk_mul_f32 v[80:81], v[96:97], v[102:103] op_sel_hi:[0,1]
	v_cmp_lt_i32_e32 vcc, v83, v101
	v_cvt_pk_f16_f32 v90, v90, v91
	v_cvt_pk_f16_f32 v91, v92, v93
	v_cvt_pk_f16_f32 v86, v86, v87
	v_cvt_pk_f16_f32 v87, v88, v89
	v_cvt_pk_f16_f32 v78, v78, v79
	v_cvt_pk_f16_f32 v79, v80, v81
	v_mov_b32_e32 v81, 0x17c00
	v_cndmask_b32_e32 v83, v95, v83, vcc
	ds_write2_b64 v100, v[90:91], v[86:87] offset1:16
	v_sub_u32_e64 v80, v123, 11 clamp
	v_lshl_or_b32 v81, v1, 7, v81
	v_lshlrev_b32_e32 v134, 2, v83
	v_or_b32_e32 v83, 64, v120
	v_mov_b32_e32 v86, 0x6d40
	v_mov_b32_e32 v87, 0xda80
	v_mov_b32_e32 v89, 0x147c0
	v_mov_b32_e32 v91, 0x1b500
	v_mov_b32_e32 v93, 0x28f80
	v_mov_b32_e32 v96, 0x2fcc0
	v_mov_b32_e32 v101, 0x3d740
	v_mov_b32_e32 v103, 0x44480
	v_mov_b32_e32 v105, 0x4b1c0
	v_mov_b32_e32 v107, 0x58c40
	v_or_b32_e32 v109, 0x3c0, v0
	v_mad_i32_i24 v80, v80, -8, v100
	v_lshrrev_b32_e32 v82, 1, v120
	v_lshl_add_u32 v139, v120, 2, v81
	v_and_or_b32 v140, v120, 48, v81
	v_lshlrev_b32_e32 v81, 3, v120
	v_mul_u32_u24_e32 v84, 0x1b5, v83
	v_lshl_add_u32 v85, v83, 3, v131
	v_mad_u32_u24 v86, v83, s10, v86
	v_mad_u32_u24 v87, v83, s10, v87
	v_mad_u32_u24 v89, v83, s10, v89
	v_mad_u32_u24 v91, v83, s10, v91
	v_mad_u32_u24 v93, v83, s10, v93
	v_mad_u32_u24 v96, v83, s10, v96
	v_mad_u32_u24 v99, v83, s10, v99
	v_mad_u32_u24 v101, v83, s10, v101
	v_mad_u32_u24 v103, v83, s10, v103
	v_mad_u32_u24 v105, v83, s10, v105
	v_mad_u32_u24 v107, v83, s10, v107
	v_mul_u32_u24_e32 v110, 0x1b5, v109
	v_mad_u32_u24 v111, v83, s10, v111
	v_mad_u32_u24 v113, v83, s10, v113
	v_mad_u32_u24 v83, v83, s10, v115
	ds_write_b64 v80, v[78:79] offset:512
	v_mul_u32_u24_e32 v78, 0x260, v123
	v_and_b32_e32 v82, 24, v82
	v_lshrrev_b32_e32 v84, 12, v84
	v_add_u32_e32 v141, v131, v81
	v_lshrrev_b32_e32 v86, 12, v86
	v_lshrrev_b32_e32 v87, 12, v87
	v_lshrrev_b32_e32 v89, 12, v89
	v_lshrrev_b32_e32 v91, 12, v91
	v_lshrrev_b32_e32 v93, 12, v93
	v_lshrrev_b32_e32 v96, 12, v96
	v_lshrrev_b32_e32 v99, 12, v99
	v_lshrrev_b32_e32 v101, 12, v101
	v_lshrrev_b32_e32 v103, 12, v103
	v_lshrrev_b32_e32 v105, 12, v105
	v_lshrrev_b32_e32 v107, 12, v107
	v_lshrrev_b32_e32 v110, 12, v110
	v_lshrrev_b32_e32 v111, 12, v111
	v_lshrrev_b32_e32 v113, 12, v113
	v_lshrrev_b32_e32 v83, 12, v83
	v_and_b32_e32 v79, 48, v0
	v_mad_u32_u24 v80, v98, s8, v131
	v_and_b32_e32 v84, 8, v84
	v_add_u32_e32 v81, 0x400, v141
	v_and_b32_e32 v86, 24, v86
	v_add_u32_e32 v88, 0x600, v141
	v_and_b32_e32 v87, 24, v87
	v_add_u32_e32 v90, 0x800, v141
	v_and_b32_e32 v89, 56, v89
	v_add_u32_e32 v92, 0xa00, v141
	v_and_b32_e32 v91, 56, v91
	v_add_u32_e32 v95, 0xe00, v141
	v_and_b32_e32 v93, 56, v93
	v_add_u32_e32 v98, 0x1000, v141
	v_and_b32_e32 v96, 56, v96
	v_add_u32_e32 v100, 0x1200, v141
	v_and_b32_e32 v99, 0x78, v99
	v_add_u32_e32 v102, 0x1400, v141
	v_and_b32_e32 v101, 0x78, v101
	v_add_u32_e32 v104, 0x1600, v141
	v_and_b32_e32 v103, 0x58, v103
	v_add_u32_e32 v106, 0x1800, v141
	v_and_b32_e32 v105, 0x58, v105
	v_add_u32_e32 v108, 0x1c00, v141
	v_and_b32_e32 v107, 0x78, v107
	v_lshl_add_u32 v109, v109, 3, v131
	v_and_b32_e32 v110, 0x78, v110
	v_add_u32_e32 v112, 0x2000, v141
	v_and_b32_e32 v111, 0x78, v111
	v_add_u32_e32 v114, 0x2200, v141
	v_and_b32_e32 v113, 0x78, v113
	v_add_u32_e32 v115, 0x2400, v141
	v_and_b32_e32 v83, 0xf8, v83
	s_movk_i32 s10, 0x4c00
	v_add_u32_e32 v78, v78, v82
	v_mad_u32_u24 v136, v123, s8, v79
	v_cmp_gt_u32_e64 s[8:9], 24, v120
	v_add3_u32 v142, v80, v79, s10
	v_add_u32_e32 v143, v85, v84
	v_add_u32_e32 v144, v81, v86
	v_add_u32_e32 v145, v88, v87
	v_add_u32_e32 v146, v90, v89
	v_add_u32_e32 v147, v92, v91
	v_add_u32_e32 v148, v95, v93
	v_add_u32_e32 v149, v98, v96
	v_add_u32_e32 v150, v100, v99
	v_add_u32_e32 v151, v102, v101
	v_add_u32_e32 v152, v104, v103
	v_add_u32_e32 v153, v106, v105
	v_add_u32_e32 v154, v108, v107
	v_add_u32_e32 v155, v109, v110
	v_add_u32_e32 v156, v112, v111
	v_add_u32_e32 v157, v114, v113
	v_add_u32_e32 v158, v115, v83
	v_add_u32_e32 v159, v80, v82
	v_add_u32_e32 v160, 64, v78
	v_mov_b32_e32 v96, 0xc604b4df
	v_mov_b32_e32 v95, v94
	v_mov_b32_e32 v98, v94
	v_mov_b32_e32 v99, v94
	v_mov_b32_e32 v100, v94
	v_mov_b32_e32 v101, v94
	v_mov_b32_e32 v102, v94
	v_mov_b32_e32 v103, v94
	v_mov_b32_e32 v104, v94
	v_mov_b32_e32 v105, v94
	v_mov_b32_e32 v106, v94
	v_mov_b32_e32 v107, v94
	v_mov_b32_e32 v108, v94
	v_mov_b32_e32 v109, v94
	v_mov_b32_e32 v110, v94
	v_mov_b32_e32 v111, v94
	v_mov_b32_e32 v112, v94
	v_mov_b32_e32 v113, v94
	v_mov_b32_e32 v114, v94
	v_mov_b32_e32 v115, v94
	v_mov_b32_e32 v117, v94
	s_waitcnt lgkmcnt(0)
	s_barrier
.LBB0_3:
	s_cmp_eq_u32 s3, 0
	s_cselect_b64 s[10:11], -1, 0
	s_cmp_eq_u32 s3, 0
	s_cbranch_scc1 .LBB0_17
	s_cmp_eq_u32 s3, 1
	s_cbranch_scc1 .Lconv_t1
	s_branch .LBB0_14
.LBB0_6:
	s_movk_i32 s12, 0x2580
	v_add_u32_e32 v70, s12, v137
	v_add_u32_e32 v71, v70, v132
	v_add_u32_e32 v66, 0x1000, v71
	buffer_load_dwordx4 v[2:5], v71, s[16:19], 0 offen nt
	buffer_load_dwordx4 v[14:17], v71, s[16:19], 0 offen offset:1024 nt
	buffer_load_dwordx4 v[34:37], v71, s[16:19], 0 offen offset:2048 nt
	buffer_load_dwordx4 v[46:49], v71, s[16:19], 0 offen offset:3072 nt
	buffer_load_dwordx4 v[54:57], v66, s[16:19], 0 offen nt
	buffer_load_dwordx4 v[58:61], v66, s[16:19], 0 offen offset:1024 nt
	buffer_load_dwordx4 v[62:65], v66, s[16:19], 0 offen offset:2048 nt
	s_nop 0
	buffer_load_dwordx4 v[66:69], v66, s[16:19], 0 offen offset:3072 nt
	v_add_u32_e32 v71, 0x2000, v71
	v_add_u32_e32 v74, v138, v70
	buffer_load_dwordx4 v[70:73], v71, s[16:19], 0 offen nt
	s_nop 0
	buffer_load_dwordx4 v[74:77], v74, s[16:19], 0 offen nt

.LBB0_16:
	s_or_b64 exec, exec, s[12:13]
	s_branch .LBB0_7
.Lconv_t1:
	s_waitcnt vmcnt(19)
	v_cvt_pk_f16_f32 v79, v188, v189
	v_cvt_pk_f16_f32 v78, v186, v187
	ds_write_b64 v141, v[78:79] offset:19456
	s_waitcnt vmcnt(18)
	v_cvt_pk_f16_f32 v79, v192, v193
	v_cvt_pk_f16_f32 v78, v190, v191
	ds_write_b64 v143, v[78:79] offset:19456
	s_waitcnt vmcnt(17)
	v_cvt_pk_f16_f32 v79, v196, v197
	v_cvt_pk_f16_f32 v78, v194, v195
	ds_write_b64 v144, v[78:79] offset:19456
	s_waitcnt vmcnt(16)
	v_cvt_pk_f16_f32 v79, v200, v201
	v_cvt_pk_f16_f32 v78, v198, v199
	ds_write_b64 v145, v[78:79] offset:19456
	s_waitcnt vmcnt(15)
	v_cvt_pk_f16_f32 v79, v204, v205
	v_cvt_pk_f16_f32 v78, v202, v203
	ds_write_b64 v146, v[78:79] offset:19456
	s_waitcnt vmcnt(14)
	v_cvt_pk_f16_f32 v79, v208, v209
	v_cvt_pk_f16_f32 v78, v206, v207
	ds_write_b64 v147, v[78:79] offset:19456
	s_waitcnt vmcnt(13)
	v_cvt_pk_f16_f32 v79, v212, v213
	v_cvt_pk_f16_f32 v78, v210, v211
	ds_write_b64 v141, v[78:79] offset:22568
	s_waitcnt vmcnt(12)
	v_cvt_pk_f16_f32 v79, v216, v217
	v_cvt_pk_f16_f32 v78, v214, v215
	ds_write_b64 v148, v[78:79] offset:19456
	s_waitcnt vmcnt(11)
	v_cvt_pk_f16_f32 v79, v220, v221
	v_cvt_pk_f16_f32 v78, v218, v219
	ds_write_b64 v149, v[78:79] offset:19456
	s_and_saveexec_b64 s[12:13], s[8:9]
	s_cbranch_execz .Lconv_t1_end
	s_waitcnt vmcnt(10)
	v_cvt_pk_f16_f32 v79, v224, v225
	v_cvt_pk_f16_f32 v78, v222, v223
	ds_write_b64 v150, v[78:79] offset:19456

.LBB0_17:
	s_waitcnt vmcnt(28)
	v_cvt_pk_f16_f32 v78, v2, v3
	v_cvt_pk_f16_f32 v79, v4, v5
	ds_write_b64 v141, v[78:79] offset:19456
	s_waitcnt vmcnt(27)
	v_cvt_pk_f16_f32 v78, v14, v15
	v_cvt_pk_f16_f32 v79, v16, v17
	ds_write_b64 v143, v[78:79] offset:19456
	s_waitcnt vmcnt(26)
	v_cvt_pk_f16_f32 v78, v34, v35
	v_cvt_pk_f16_f32 v79, v36, v37
	ds_write_b64 v144, v[78:79] offset:19456
	s_waitcnt vmcnt(25)
	v_cvt_pk_f16_f32 v78, v46, v47
	v_cvt_pk_f16_f32 v79, v48, v49
	ds_write_b64 v145, v[78:79] offset:19456
	s_waitcnt vmcnt(24)
	v_cvt_pk_f16_f32 v78, v54, v55
	v_cvt_pk_f16_f32 v79, v56, v57
	ds_write_b64 v146, v[78:79] offset:19456
	s_waitcnt vmcnt(23)
	v_cvt_pk_f16_f32 v78, v58, v59
	v_cvt_pk_f16_f32 v79, v60, v61
	ds_write_b64 v147, v[78:79] offset:19456
	s_waitcnt vmcnt(22)
	v_cvt_pk_f16_f32 v78, v62, v63
	v_cvt_pk_f16_f32 v79, v64, v65
	ds_write_b64 v141, v[78:79] offset:22568
	s_waitcnt vmcnt(21)
	v_cvt_pk_f16_f32 v78, v66, v67
	v_cvt_pk_f16_f32 v79, v68, v69
	ds_write_b64 v148, v[78:79] offset:19456
	s_waitcnt vmcnt(20)
	v_cvt_pk_f16_f32 v78, v70, v71
	v_cvt_pk_f16_f32 v79, v72, v73
	ds_write_b64 v149, v[78:79] offset:19456
	s_waitcnt vmcnt(19)
	v_cvt_pk_f16_f32 v78, v74, v75
	v_cvt_pk_f16_f32 v79, v76, v77
	ds_write_b64 v150, v[78:79] offset:19456
	s_waitcnt vmcnt(18)
	v_cvt_pk_f16_f32 v78, v6, v7
	v_cvt_pk_f16_f32 v79, v8, v9
	ds_write_b64 v151, v[78:79] offset:19456
	s_waitcnt vmcnt(17)
	v_cvt_pk_f16_f32 v78, v10, v11
	v_cvt_pk_f16_f32 v79, v12, v13
	ds_write_b64 v152, v[78:79] offset:19456
	s_waitcnt vmcnt(16)
	v_cvt_pk_f16_f32 v78, v18, v19
	v_cvt_pk_f16_f32 v79, v20, v21
	ds_write_b64 v153, v[78:79] offset:19456
	s_waitcnt vmcnt(15)
	v_cvt_pk_f16_f32 v78, v22, v23
	v_cvt_pk_f16_f32 v79, v24, v25
	ds_write_b64 v141, v[78:79] offset:26200
	s_waitcnt vmcnt(14)
	v_cvt_pk_f16_f32 v78, v26, v27
	v_cvt_pk_f16_f32 v79, v28, v29
	ds_write_b64 v154, v[78:79] offset:19456
	s_waitcnt vmcnt(13)
	v_cvt_pk_f16_f32 v78, v30, v31
	v_cvt_pk_f16_f32 v79, v32, v33
	ds_write_b64 v155, v[78:79] offset:19456
	s_waitcnt vmcnt(12)
	v_cvt_pk_f16_f32 v78, v38, v39
	v_cvt_pk_f16_f32 v79, v40, v41
	ds_write_b64 v156, v[78:79] offset:19456
	s_waitcnt vmcnt(11)
	v_cvt_pk_f16_f32 v78, v42, v43
	v_cvt_pk_f16_f32 v79, v44, v45
	ds_write_b64 v157, v[78:79] offset:19456
	s_waitcnt vmcnt(10)
	v_cvt_pk_f16_f32 v78, v50, v51
	v_cvt_pk_f16_f32 v79, v52, v53
	s_and_saveexec_b64 s[12:13], s[6:7]
	ds_write_b64 v158, v[78:79] offset:19456
	s_or_b64 exec, exec, s[12:13]
	s_branch .LBB0_6
.LBB0_20:
	v_lshlrev_b32_e32 v2, 2, v123
	v_lshl_add_u32 v3, v120, 2, v131
	ds_write2st64_b32 v3, v94, v95 offset0:76 offset1:77
	ds_write2st64_b32 v3, v98, v99 offset0:78 offset1:79
	ds_write2st64_b32 v3, v100, v101 offset0:80 offset1:81
	ds_write2st64_b32 v3, v102, v103 offset0:82 offset1:83
	ds_write2st64_b32 v3, v104, v105 offset0:84 offset1:85
	ds_write2st64_b32 v3, v106, v107 offset0:86 offset1:87
	ds_write2st64_b32 v3, v108, v109 offset0:88 offset1:89
	ds_write2st64_b32 v3, v110, v111 offset0:90 offset1:91
	ds_write2st64_b32 v3, v112, v113 offset0:92 offset1:93
	ds_write2st64_b32 v3, v114, v115 offset0:94 offset1:95
	ds_write2st64_b32 v3, v116, v117 offset0:96 offset1:97
	v_mov_b32_e32 v3, 0
	s_waitcnt lgkmcnt(0)
	s_barrier
	s_and_saveexec_b64 s[4:5], s[0:1]
	s_cbranch_execz .LBB0_22
	s_waitcnt vmcnt(8)
	v_lshlrev_b32_e32 v8, 1, v121
	v_lshrrev_b32_e32 v3, 4, v122
	v_or_b32_e32 v3, v8, v3
	v_lshl_or_b32 v9, v3, 8, v2
	s_waitcnt vmcnt(7)
	v_add_u32_e32 v10, 0x4c00, v9
	ds_read2_b32 v[2:3], v10 offset1:16
	ds_read2_b32 v[4:5], v10 offset0:32 offset1:48
	v_add_u32_e32 v11, 0x7000, v9
	ds_read2_b32 v[6:7], v11 offset0:128 offset1:144
	v_cmp_lt_u32_e32 vcc, 31, v0
	s_waitcnt lgkmcnt(2)
	v_add_f32_e32 v2, 0, v2
	v_add_f32_e32 v2, v2, v3
	s_waitcnt lgkmcnt(1)
	v_add_f32_e32 v2, v2, v4
	v_add_f32_e32 v12, v2, v5
	ds_read2_b32 v[2:3], v11 offset0:160 offset1:176
	v_add_u32_e32 v11, 0x9800, v9
	ds_read2_b32 v[4:5], v11 offset1:16
	s_waitcnt lgkmcnt(2)
	v_add_f32_e32 v6, v12, v6
	v_add_f32_e32 v6, v6, v7
	s_waitcnt lgkmcnt(1)
	v_add_f32_e32 v2, v6, v2
	v_add_f32_e32 v2, v2, v3
	s_waitcnt lgkmcnt(0)
	v_add_f32_e32 v4, v2, v4
	ds_read2_b32 v[2:3], v11 offset0:32 offset1:48
	v_add_u32_e32 v11, 0xbc00, v9
	ds_read2_b32 v[6:7], v11 offset0:128 offset1:144
	v_add_f32_e32 v12, v4, v5
	ds_read2_b32 v[4:5], v11 offset0:160 offset1:176
	s_waitcnt lgkmcnt(2)
	v_add_f32_e32 v2, v12, v2
	v_add_f32_e32 v2, v2, v3
	s_waitcnt lgkmcnt(1)
	v_add_f32_e32 v2, v2, v6
	v_add_f32_e32 v2, v2, v7
	v_add_u32_e32 v6, 0xe400, v9
	s_waitcnt lgkmcnt(0)
	v_add_f32_e32 v4, v2, v4
	ds_read2_b32 v[2:3], v6 offset1:16
	v_add_f32_e32 v11, v4, v5
	ds_read2_b32 v[4:5], v6 offset0:32 offset1:48
	v_add_u32_e32 v12, 0xbc00, v10
	ds_read2_b32 v[6:7], v12 offset0:128 offset1:144
	s_waitcnt lgkmcnt(2)
	v_add_f32_e32 v2, v11, v2
	v_add_f32_e32 v2, v2, v3
	s_waitcnt lgkmcnt(1)
	v_add_f32_e32 v2, v2, v4
	v_add_f32_e32 v2, v2, v5
	s_waitcnt lgkmcnt(0)
	v_add_f32_e32 v6, v2, v6
	ds_read2_b32 v[2:3], v12 offset0:160 offset1:176
	v_add_u32_e32 v10, 0xe400, v10
	ds_read2_b32 v[4:5], v10 offset1:16
	v_add_f32_e32 v11, v6, v7
	ds_read2_b32 v[6:7], v10 offset0:32 offset1:48
	s_waitcnt lgkmcnt(2)
	v_add_f32_e32 v2, v11, v2
	v_add_f32_e32 v2, v2, v3
	s_waitcnt lgkmcnt(1)
	v_add_f32_e32 v2, v2, v4
	v_add_f32_e32 v2, v2, v5
	s_waitcnt lgkmcnt(0)
	v_add_f32_e32 v2, v2, v6
	v_add_f32_e32 v2, v2, v7
	v_add_u32_e32 v3, 0x15600, v9
	v_add_u32_e32 v4, 0x15640, v9
	v_sub_u32_e32 v7, 11, v8
	ds_read_b32 v3, v3
	ds_read_b32 v4, v4
	v_cvt_f32_i32_e32 v7, v7
	v_add_u32_e32 v5, 0x15680, v9
	v_add_u32_e32 v6, 0x156c0, v9
	s_waitcnt lgkmcnt(1)
	v_add_f32_e32 v2, v2, v3
	v_mul_f32_e32 v3, 0xbf38aa3b, v7
	ds_read_b32 v5, v5
	ds_read_b32 v6, v6
	v_mul_f32_e32 v3, v3, v7
	v_exp_f32_e32 v3, v3
	s_waitcnt lgkmcnt(2)
	v_add_f32_e32 v2, v2, v4
	s_waitcnt lgkmcnt(1)
	v_add_f32_e32 v2, v2, v5
	s_waitcnt lgkmcnt(0)
	v_add_f32_e32 v2, v2, v6
	v_cndmask_b32_e32 v3, 1.0, v3, vcc
	v_mul_f32_e32 v2, v3, v2
	v_max_f32_e32 v2, 0x2edbe6ff, v2
	v_log_f32_e32 v2, v2
	v_cmp_lt_i32_e32 vcc, 1, v119
	v_mul_f32_e32 v2, v118, v2
	s_nop 0
	v_cndmask_b32_e32 v3, 0, v2, vcc

	.amdhsa_kernel _Z11knrm_kernelPKfS0_PKiS2_S0_Pf
		.amdhsa_group_segment_fixed_size 99712
		.amdhsa_private_segment_fixed_size 0
		.amdhsa_kernarg_size 48
		.amdhsa_user_sgpr_count 2
		.amdhsa_user_sgpr_dispatch_ptr 0
		.amdhsa_user_sgpr_queue_ptr 0
		.amdhsa_user_sgpr_kernarg_segment_ptr 1
		.amdhsa_user_sgpr_dispatch_id 0
		.amdhsa_user_sgpr_kernarg_preload_length 0
		.amdhsa_user_sgpr_kernarg_preload_offset 0
		.amdhsa_user_sgpr_private_segment_size 0
		.amdhsa_uses_dynamic_stack 0
		.amdhsa_enable_private_segment 0
		.amdhsa_system_sgpr_workgroup_id_x 1
		.amdhsa_system_sgpr_workgroup_id_y 0
		.amdhsa_system_sgpr_workgroup_id_z 0
		.amdhsa_system_sgpr_workgroup_info 0
		.amdhsa_system_vgpr_workitem_id 0
		.amdhsa_next_free_vgpr 230
		.amdhsa_next_free_sgpr 96
		.amdhsa_accum_offset 232
		.amdhsa_reserve_vcc 1
		.amdhsa_float_round_mode_32 0
		.amdhsa_float_round_mode_16_64 0
		.amdhsa_float_denorm_mode_32 3
		.amdhsa_float_denorm_mode_16_64 3
		.amdhsa_dx10_clamp 1
		.amdhsa_ieee_mode 1
		.amdhsa_fp16_overflow 0
		.amdhsa_tg_split 0
		.amdhsa_exception_fp_ieee_invalid_op 0
		.amdhsa_exception_fp_denorm_src 0
		.amdhsa_exception_fp_ieee_div_zero 0
		.amdhsa_exception_fp_ieee_overflow 0
		.amdhsa_exception_fp_ieee_underflow 0
		.amdhsa_exception_fp_ieee_inexact 0
		.amdhsa_exception_int_div_zero 0
	.end_amdhsa_kernel

amdhsa.kernels:
  - .agpr_count:     0
    .args:
      - .actual_access:  read_only
        .address_space:  global
        .offset:         0
        .size:           8
        .value_kind:     global_buffer
      - .actual_access:  read_only
        .address_space:  global
        .offset:         8
        .size:           8
        .value_kind:     global_buffer
      - .actual_access:  read_only
        .address_space:  global
        .offset:         16
        .size:           8
        .value_kind:     global_buffer
      - .actual_access:  read_only
        .address_space:  global
        .offset:         24
        .size:           8
        .value_kind:     global_buffer
      - .actual_access:  read_only
        .address_space:  global
        .offset:         32
        .size:           8
        .value_kind:     global_buffer
      - .actual_access:  write_only
        .address_space:  global
        .offset:         40
        .size:           8
        .value_kind:     global_buffer
    .group_segment_fixed_size: 99712
    .kernarg_segment_align: 8
    .kernarg_segment_size: 48
    .language:       OpenCL C
    .language_version:
      - 2
      - 0
    .max_flat_workgroup_size: 512
    .name:           _Z11knrm_kernelPKfS0_PKiS2_S0_Pf
    .private_segment_fixed_size: 0
    .sgpr_count:     32
    .sgpr_spill_count: 0
    .symbol:         _Z11knrm_kernelPKfS0_PKiS2_S0_Pf.kd
    .uniform_work_group_size: 1
    .uses_dynamic_stack: false
    .vgpr_count:     230
    .vgpr_spill_count: 0
    .wavefront_size: 64
